# speedup vs baseline: 1.0099x; 1.0099x over previous
.Lpairs_no3a:
	s_waitcnt vmcnt(16)
	ds_write_b128 v72, v[52:55]
	ds_write_b128 v72, v[56:59] offset:8192
	s_waitcnt lgkmcnt(0)
	s_barrier
	s_mov_b32 s36, s32
	s_mov_b32 s37, s33
	s_cmpk_lt_i32 s34, 0x30d4
	s_cbranch_scc0 .Lpairs_joint
	s_waitcnt vmcnt(5)
	ds_read_b128 v[52:55], v2 offset:0
	ds_read_b128 v[56:59], v2 offset:1024
	ds_read_b128 v[60:63], v2 offset:2048
	ds_read_b128 v[64:67], v2 offset:3072
	s_waitcnt lgkmcnt(3)
	v_mfma_f32_16x16x32_f16 v[16:19], v[20:23], v[52:55], 0
	ds_read_b128 v[52:55], v2 offset:4096
	s_waitcnt lgkmcnt(3)
	v_mfma_f32_16x16x32_f16 v[16:19], v[24:27], v[56:59], v[16:19]
	ds_read_b128 v[56:59], v2 offset:5120
	s_waitcnt lgkmcnt(3)
	v_mfma_f32_16x16x32_f16 v[16:19], v[28:31], v[60:63], v[16:19]
	ds_read_b128 v[60:63], v2 offset:6144
	s_waitcnt lgkmcnt(3)
	v_mfma_f32_16x16x32_f16 v[16:19], v[32:35], v[64:67], v[16:19]
	ds_read_b128 v[64:67], v2 offset:7168
	s_nop 7
	v_add_f32_e32 v16, v4, v16
	v_add_f32_e32 v17, v4, v17
	v_add_f32_e32 v18, v4, v18
	v_add_f32_e32 v19, v4, v19
	v_max_f32_e32 v16, 0, v16
	v_max_f32_e32 v17, 0, v17
	v_max_f32_e32 v18, 0, v18
	v_max_f32_e32 v19, 0, v19
	v_mul_f32_e32 v12, v8, v16
	v_mul_f32_e32 v13, v8, v17
	v_mul_f32_e32 v14, v8, v18
	v_mul_f32_e32 v15, v8, v19
	s_waitcnt lgkmcnt(3)
	v_mfma_f32_16x16x32_f16 v[16:19], v[20:23], v[52:55], 0
	ds_read_b128 v[52:55], v2 offset:8192
	s_waitcnt lgkmcnt(3)
	v_mfma_f32_16x16x32_f16 v[16:19], v[24:27], v[56:59], v[16:19]
	ds_read_b128 v[56:59], v2 offset:9216
	s_waitcnt lgkmcnt(3)
	v_mfma_f32_16x16x32_f16 v[16:19], v[28:31], v[60:63], v[16:19]
	ds_read_b128 v[60:63], v2 offset:10240
	s_waitcnt lgkmcnt(3)
	v_mfma_f32_16x16x32_f16 v[16:19], v[32:35], v[64:67], v[16:19]
	ds_read_b128 v[64:67], v2 offset:11264
	s_nop 7
	v_add_f32_e32 v16, v5, v16
	v_add_f32_e32 v17, v5, v17
	v_add_f32_e32 v18, v5, v18
	v_add_f32_e32 v19, v5, v19
	v_max_f32_e32 v16, 0, v16
	v_max_f32_e32 v17, 0, v17
	v_max_f32_e32 v18, 0, v18
	v_max_f32_e32 v19, 0, v19
	v_fmac_f32_e32 v12, v9, v16
	v_fmac_f32_e32 v13, v9, v17
	v_fmac_f32_e32 v14, v9, v18
	v_fmac_f32_e32 v15, v9, v19
	s_waitcnt lgkmcnt(3)
	v_mfma_f32_16x16x32_f16 v[16:19], v[20:23], v[52:55], 0
	ds_read_b128 v[52:55], v2 offset:12288
	s_waitcnt lgkmcnt(3)
	v_mfma_f32_16x16x32_f16 v[16:19], v[24:27], v[56:59], v[16:19]
	ds_read_b128 v[56:59], v2 offset:13312
	s_waitcnt lgkmcnt(3)
	v_mfma_f32_16x16x32_f16 v[16:19], v[28:31], v[60:63], v[16:19]
	ds_read_b128 v[60:63], v2 offset:14336
	s_waitcnt lgkmcnt(3)
	v_mfma_f32_16x16x32_f16 v[16:19], v[32:35], v[64:67], v[16:19]
	ds_read_b128 v[64:67], v2 offset:15360
	s_nop 7
	v_add_f32_e32 v16, v6, v16
	v_add_f32_e32 v17, v6, v17
	v_add_f32_e32 v18, v6, v18
	v_add_f32_e32 v19, v6, v19
	v_max_f32_e32 v16, 0, v16
	v_max_f32_e32 v17, 0, v17
	v_max_f32_e32 v18, 0, v18
	v_max_f32_e32 v19, 0, v19
	v_fmac_f32_e32 v12, v10, v16
	v_fmac_f32_e32 v13, v10, v17
	v_fmac_f32_e32 v14, v10, v18
	v_fmac_f32_e32 v15, v10, v19
	s_waitcnt lgkmcnt(3)
	v_mfma_f32_16x16x32_f16 v[16:19], v[20:23], v[52:55], 0
	s_waitcnt lgkmcnt(2)
	v_mfma_f32_16x16x32_f16 v[16:19], v[24:27], v[56:59], v[16:19]
	s_waitcnt lgkmcnt(1)
	v_mfma_f32_16x16x32_f16 v[16:19], v[28:31], v[60:63], v[16:19]
	s_waitcnt lgkmcnt(0)
	v_mfma_f32_16x16x32_f16 v[16:19], v[32:35], v[64:67], v[16:19]
	s_nop 7
	v_add_f32_e32 v16, v7, v16
	v_add_f32_e32 v17, v7, v17
	v_add_f32_e32 v18, v7, v18
	v_add_f32_e32 v19, v7, v19
	v_max_f32_e32 v16, 0, v16
	v_max_f32_e32 v17, 0, v17
	v_max_f32_e32 v18, 0, v18
	v_max_f32_e32 v19, 0, v19
	v_fmac_f32_e32 v12, v11, v16
	v_fmac_f32_e32 v13, v11, v17
	v_fmac_f32_e32 v14, v11, v18
	v_fmac_f32_e32 v15, v11, v19
	v_add_f32_dpp v12, v12, v12 quad_perm:[1,0,3,2] row_mask:0xf bank_mask:0xf
	v_add_f32_dpp v13, v13, v13 quad_perm:[1,0,3,2] row_mask:0xf bank_mask:0xf
	v_add_f32_dpp v14, v14, v14 quad_perm:[1,0,3,2] row_mask:0xf bank_mask:0xf
	v_add_f32_dpp v15, v15, v15 quad_perm:[1,0,3,2] row_mask:0xf bank_mask:0xf
	v_add_f32_dpp v12, v12, v12 quad_perm:[2,3,0,1] row_mask:0xf bank_mask:0xf
	v_add_f32_dpp v13, v13, v13 quad_perm:[2,3,0,1] row_mask:0xf bank_mask:0xf
	v_add_f32_dpp v14, v14, v14 quad_perm:[2,3,0,1] row_mask:0xf bank_mask:0xf
	v_add_f32_dpp v15, v15, v15 quad_perm:[2,3,0,1] row_mask:0xf bank_mask:0xf
	v_add_f32_dpp v12, v12, v12 row_half_mirror row_mask:0xf bank_mask:0xf
	v_add_f32_dpp v13, v13, v13 row_half_mirror row_mask:0xf bank_mask:0xf
	v_add_f32_dpp v14, v14, v14 row_half_mirror row_mask:0xf bank_mask:0xf
	v_add_f32_dpp v15, v15, v15 row_half_mirror row_mask:0xf bank_mask:0xf
	v_add_f32_dpp v12, v12, v12 row_mirror row_mask:0xf bank_mask:0xf
	v_add_f32_dpp v13, v13, v13 row_mirror row_mask:0xf bank_mask:0xf
	v_add_f32_dpp v14, v14, v14 row_mirror row_mask:0xf bank_mask:0xf
	v_add_f32_dpp v15, v15, v15 row_mirror row_mask:0xf bank_mask:0xf
	s_lshl_b32 s3, s36, 6
	s_add_u32 s24, s16, s3
	s_addc_u32 s25, s17, 0
	v_cndmask_b32_e64 v12, v12, v13, s[20:21]
	s_nop 0
	v_cndmask_b32_e64 v12, v12, v14, s[22:23]
	s_nop 0
	v_cndmask_b32_e64 v12, v12, v15, s[26:27]
	s_nop 0
	v_add_f32_e32 v12, s18, v12
	s_mov_b64 s[30:31], exec
	s_mov_b64 exec, s[28:29]
	global_store_dword v0, v12, s[24:25]
	s_mov_b64 exec, s[30:31]
	s_waitcnt vmcnt(0)
	v_lshl_or_b32 v70, v68, 7, v76
	v_lshl_or_b32 v71, v69, 7, v76
	global_load_dwordx4 v[20:23], v70, s[4:5]
	global_load_dwordx4 v[24:27], v70, s[4:5] offset:64
	global_load_dwordx4 v[28:31], v71, s[4:5]
	global_load_dwordx4 v[32:35], v71, s[4:5] offset:64
	s_mov_b32 s36, s34
.Lpairs_joint:
	s_waitcnt vmcnt(0)
	ds_read_b128 v[52:55], v2 offset:0
	ds_read_b128 v[56:59], v2 offset:1024
	ds_read_b128 v[60:63], v2 offset:2048
	ds_read_b128 v[64:67], v2 offset:3072
	s_waitcnt lgkmcnt(3)
	v_mfma_f32_16x16x32_f16 v[16:19], v[20:23], v[52:55], 0
	v_mfma_f32_16x16x32_f16 v[72:75], v[36:39], v[52:55], 0
	ds_read_b128 v[52:55], v2 offset:4096
	s_waitcnt lgkmcnt(3)
	v_mfma_f32_16x16x32_f16 v[16:19], v[24:27], v[56:59], v[16:19]
	v_mfma_f32_16x16x32_f16 v[72:75], v[40:43], v[56:59], v[72:75]
	ds_read_b128 v[56:59], v2 offset:5120
	s_waitcnt lgkmcnt(3)
	v_mfma_f32_16x16x32_f16 v[16:19], v[28:31], v[60:63], v[16:19]
	v_mfma_f32_16x16x32_f16 v[72:75], v[44:47], v[60:63], v[72:75]
	ds_read_b128 v[60:63], v2 offset:6144
	s_waitcnt lgkmcnt(3)
	v_mfma_f32_16x16x32_f16 v[16:19], v[32:35], v[64:67], v[16:19]
	v_mfma_f32_16x16x32_f16 v[72:75], v[48:51], v[64:67], v[72:75]
	ds_read_b128 v[64:67], v2 offset:7168
	s_nop 7
	v_add_f32_e32 v16, v4, v16
	v_add_f32_e32 v17, v4, v17
	v_add_f32_e32 v18, v4, v18
	v_add_f32_e32 v19, v4, v19
	v_max_f32_e32 v16, 0, v16
	v_max_f32_e32 v17, 0, v17
	v_max_f32_e32 v18, 0, v18
	v_max_f32_e32 v19, 0, v19
	v_mul_f32_e32 v12, v8, v16
	v_mul_f32_e32 v13, v8, v17
	v_mul_f32_e32 v14, v8, v18
	v_mul_f32_e32 v15, v8, v19
	v_add_f32_e32 v72, v4, v72
	v_add_f32_e32 v73, v4, v73
	v_add_f32_e32 v74, v4, v74
	v_add_f32_e32 v75, v4, v75
	v_max_f32_e32 v72, 0, v72
	v_max_f32_e32 v73, 0, v73
	v_max_f32_e32 v74, 0, v74
	v_max_f32_e32 v75, 0, v75
	v_mul_f32_e32 v3, v8, v72
	v_mul_f32_e32 v77, v8, v73
	v_mul_f32_e32 v70, v8, v74
	v_mul_f32_e32 v71, v8, v75
	s_waitcnt lgkmcnt(3)
	v_mfma_f32_16x16x32_f16 v[16:19], v[20:23], v[52:55], 0
	v_mfma_f32_16x16x32_f16 v[72:75], v[36:39], v[52:55], 0
	ds_read_b128 v[52:55], v2 offset:8192
	s_waitcnt lgkmcnt(3)
	v_mfma_f32_16x16x32_f16 v[16:19], v[24:27], v[56:59], v[16:19]
	v_mfma_f32_16x16x32_f16 v[72:75], v[40:43], v[56:59], v[72:75]
	ds_read_b128 v[56:59], v2 offset:9216
	s_waitcnt lgkmcnt(3)
	v_mfma_f32_16x16x32_f16 v[16:19], v[28:31], v[60:63], v[16:19]
	v_mfma_f32_16x16x32_f16 v[72:75], v[44:47], v[60:63], v[72:75]
	ds_read_b128 v[60:63], v2 offset:10240
	s_waitcnt lgkmcnt(3)
	v_mfma_f32_16x16x32_f16 v[16:19], v[32:35], v[64:67], v[16:19]
	v_mfma_f32_16x16x32_f16 v[72:75], v[48:51], v[64:67], v[72:75]
	ds_read_b128 v[64:67], v2 offset:11264
	s_nop 7
	v_add_f32_e32 v16, v5, v16
	v_add_f32_e32 v17, v5, v17
	v_add_f32_e32 v18, v5, v18
	v_add_f32_e32 v19, v5, v19
	v_max_f32_e32 v16, 0, v16
	v_max_f32_e32 v17, 0, v17
	v_max_f32_e32 v18, 0, v18
	v_max_f32_e32 v19, 0, v19
	v_fmac_f32_e32 v12, v9, v16
	v_fmac_f32_e32 v13, v9, v17
	v_fmac_f32_e32 v14, v9, v18
	v_fmac_f32_e32 v15, v9, v19
	v_add_f32_e32 v72, v5, v72
	v_add_f32_e32 v73, v5, v73
	v_add_f32_e32 v74, v5, v74
	v_add_f32_e32 v75, v5, v75
	v_max_f32_e32 v72, 0, v72
	v_max_f32_e32 v73, 0, v73
	v_max_f32_e32 v74, 0, v74
	v_max_f32_e32 v75, 0, v75
	v_fmac_f32_e32 v3, v9, v72
	v_fmac_f32_e32 v77, v9, v73
	v_fmac_f32_e32 v70, v9, v74
	v_fmac_f32_e32 v71, v9, v75
	s_waitcnt lgkmcnt(3)
	v_mfma_f32_16x16x32_f16 v[16:19], v[20:23], v[52:55], 0
	v_mfma_f32_16x16x32_f16 v[72:75], v[36:39], v[52:55], 0
	ds_read_b128 v[52:55], v2 offset:12288
	s_waitcnt lgkmcnt(3)
	v_mfma_f32_16x16x32_f16 v[16:19], v[24:27], v[56:59], v[16:19]
	v_mfma_f32_16x16x32_f16 v[72:75], v[40:43], v[56:59], v[72:75]
	ds_read_b128 v[56:59], v2 offset:13312
	s_waitcnt lgkmcnt(3)
	v_mfma_f32_16x16x32_f16 v[16:19], v[28:31], v[60:63], v[16:19]
	v_mfma_f32_16x16x32_f16 v[72:75], v[44:47], v[60:63], v[72:75]
	ds_read_b128 v[60:63], v2 offset:14336
	s_waitcnt lgkmcnt(3)
	v_mfma_f32_16x16x32_f16 v[16:19], v[32:35], v[64:67], v[16:19]
	v_mfma_f32_16x16x32_f16 v[72:75], v[48:51], v[64:67], v[72:75]
	ds_read_b128 v[64:67], v2 offset:15360
	s_nop 7
	v_add_f32_e32 v16, v6, v16
	v_add_f32_e32 v17, v6, v17
	v_add_f32_e32 v18, v6, v18
	v_add_f32_e32 v19, v6, v19
	v_max_f32_e32 v16, 0, v16
	v_max_f32_e32 v17, 0, v17
	v_max_f32_e32 v18, 0, v18
	v_max_f32_e32 v19, 0, v19
	v_fmac_f32_e32 v12, v10, v16
	v_fmac_f32_e32 v13, v10, v17
	v_fmac_f32_e32 v14, v10, v18
	v_fmac_f32_e32 v15, v10, v19
	v_add_f32_e32 v72, v6, v72
	v_add_f32_e32 v73, v6, v73
	v_add_f32_e32 v74, v6, v74
	v_add_f32_e32 v75, v6, v75
	v_max_f32_e32 v72, 0, v72
	v_max_f32_e32 v73, 0, v73
	v_max_f32_e32 v74, 0, v74
	v_max_f32_e32 v75, 0, v75
	v_fmac_f32_e32 v3, v10, v72
	v_fmac_f32_e32 v77, v10, v73
	v_fmac_f32_e32 v70, v10, v74
	v_fmac_f32_e32 v71, v10, v75
	s_waitcnt lgkmcnt(3)
	v_mfma_f32_16x16x32_f16 v[16:19], v[20:23], v[52:55], 0
	v_mfma_f32_16x16x32_f16 v[72:75], v[36:39], v[52:55], 0
	s_waitcnt lgkmcnt(2)
	v_mfma_f32_16x16x32_f16 v[16:19], v[24:27], v[56:59], v[16:19]
	v_mfma_f32_16x16x32_f16 v[72:75], v[40:43], v[56:59], v[72:75]
	s_waitcnt lgkmcnt(1)
	v_mfma_f32_16x16x32_f16 v[16:19], v[28:31], v[60:63], v[16:19]
	v_mfma_f32_16x16x32_f16 v[72:75], v[44:47], v[60:63], v[72:75]
	s_waitcnt lgkmcnt(0)
	v_mfma_f32_16x16x32_f16 v[16:19], v[32:35], v[64:67], v[16:19]
	v_mfma_f32_16x16x32_f16 v[72:75], v[48:51], v[64:67], v[72:75]
	s_nop 7
	v_add_f32_e32 v16, v7, v16
	v_add_f32_e32 v17, v7, v17
	v_add_f32_e32 v18, v7, v18
	v_add_f32_e32 v19, v7, v19
	v_max_f32_e32 v16, 0, v16
	v_max_f32_e32 v17, 0, v17
	v_max_f32_e32 v18, 0, v18
	v_max_f32_e32 v19, 0, v19
	v_fmac_f32_e32 v12, v11, v16
	v_fmac_f32_e32 v13, v11, v17
	v_fmac_f32_e32 v14, v11, v18
	v_fmac_f32_e32 v15, v11, v19
	v_add_f32_e32 v72, v7, v72
	v_add_f32_e32 v73, v7, v73
	v_add_f32_e32 v74, v7, v74
	v_add_f32_e32 v75, v7, v75
	v_max_f32_e32 v72, 0, v72
	v_max_f32_e32 v73, 0, v73
	v_max_f32_e32 v74, 0, v74
	v_max_f32_e32 v75, 0, v75
	v_fmac_f32_e32 v3, v11, v72
	v_fmac_f32_e32 v77, v11, v73
	v_fmac_f32_e32 v70, v11, v74
	v_fmac_f32_e32 v71, v11, v75
	v_add_f32_dpp v12, v12, v12 quad_perm:[1,0,3,2] row_mask:0xf bank_mask:0xf
	v_add_f32_dpp v13, v13, v13 quad_perm:[1,0,3,2] row_mask:0xf bank_mask:0xf
	v_add_f32_dpp v14, v14, v14 quad_perm:[1,0,3,2] row_mask:0xf bank_mask:0xf
	v_add_f32_dpp v15, v15, v15 quad_perm:[1,0,3,2] row_mask:0xf bank_mask:0xf
	v_add_f32_dpp v3, v3, v3 quad_perm:[1,0,3,2] row_mask:0xf bank_mask:0xf
	v_add_f32_dpp v77, v77, v77 quad_perm:[1,0,3,2] row_mask:0xf bank_mask:0xf
	v_add_f32_dpp v70, v70, v70 quad_perm:[1,0,3,2] row_mask:0xf bank_mask:0xf
	v_add_f32_dpp v71, v71, v71 quad_perm:[1,0,3,2] row_mask:0xf bank_mask:0xf
	v_add_f32_dpp v12, v12, v12 quad_perm:[2,3,0,1] row_mask:0xf bank_mask:0xf
	v_add_f32_dpp v13, v13, v13 quad_perm:[2,3,0,1] row_mask:0xf bank_mask:0xf
	v_add_f32_dpp v14, v14, v14 quad_perm:[2,3,0,1] row_mask:0xf bank_mask:0xf
	v_add_f32_dpp v15, v15, v15 quad_perm:[2,3,0,1] row_mask:0xf bank_mask:0xf
	v_add_f32_dpp v3, v3, v3 quad_perm:[2,3,0,1] row_mask:0xf bank_mask:0xf
	v_add_f32_dpp v77, v77, v77 quad_perm:[2,3,0,1] row_mask:0xf bank_mask:0xf
	v_add_f32_dpp v70, v70, v70 quad_perm:[2,3,0,1] row_mask:0xf bank_mask:0xf
	v_add_f32_dpp v71, v71, v71 quad_perm:[2,3,0,1] row_mask:0xf bank_mask:0xf
	v_add_f32_dpp v12, v12, v12 row_half_mirror row_mask:0xf bank_mask:0xf
	v_add_f32_dpp v13, v13, v13 row_half_mirror row_mask:0xf bank_mask:0xf
	v_add_f32_dpp v14, v14, v14 row_half_mirror row_mask:0xf bank_mask:0xf
	v_add_f32_dpp v15, v15, v15 row_half_mirror row_mask:0xf bank_mask:0xf
	v_add_f32_dpp v3, v3, v3 row_half_mirror row_mask:0xf bank_mask:0xf
	v_add_f32_dpp v77, v77, v77 row_half_mirror row_mask:0xf bank_mask:0xf
	v_add_f32_dpp v70, v70, v70 row_half_mirror row_mask:0xf bank_mask:0xf
	v_add_f32_dpp v71, v71, v71 row_half_mirror row_mask:0xf bank_mask:0xf
	v_add_f32_dpp v12, v12, v12 row_mirror row_mask:0xf bank_mask:0xf
	v_add_f32_dpp v13, v13, v13 row_mirror row_mask:0xf bank_mask:0xf
	v_add_f32_dpp v14, v14, v14 row_mirror row_mask:0xf bank_mask:0xf
	v_add_f32_dpp v15, v15, v15 row_mirror row_mask:0xf bank_mask:0xf
	v_add_f32_dpp v3, v3, v3 row_mirror row_mask:0xf bank_mask:0xf
	v_add_f32_dpp v77, v77, v77 row_mirror row_mask:0xf bank_mask:0xf
	v_add_f32_dpp v70, v70, v70 row_mirror row_mask:0xf bank_mask:0xf
	v_add_f32_dpp v71, v71, v71 row_mirror row_mask:0xf bank_mask:0xf
	s_lshl_b32 s3, s36, 6
	s_add_u32 s24, s16, s3
	s_addc_u32 s25, s17, 0
	s_lshl_b32 s3, s37, 6
	s_add_u32 s2, s16, s3
	s_addc_u32 s3, s17, 0
	v_cndmask_b32_e64 v12, v12, v13, s[20:21]
	v_cndmask_b32_e64 v3, v3, v77, s[20:21]
	v_cndmask_b32_e64 v12, v12, v14, s[22:23]
	v_cndmask_b32_e64 v3, v3, v70, s[22:23]
	v_cndmask_b32_e64 v12, v12, v15, s[26:27]
	v_cndmask_b32_e64 v3, v3, v71, s[26:27]
	v_add_f32_e32 v12, s18, v12
	v_add_f32_e32 v3, s18, v3
	s_mov_b64 exec, s[28:29]
	global_store_dword v0, v12, s[24:25]
	global_store_dword v0, v3, s[2:3]
